# P9 gate/up GEMM loop: back edge rotated (operand-address selection moved before the loop-closing barrier); on top of v6
# speedup vs baseline: 1.0053x; 1.0053x over previous
.LBB0_1335:
	ds_read_b128 v[0:3], v184
	ds_read_b128 v[4:7], v189
	ds_read_b128 v[8:11], v190
	ds_read_b128 v[12:15], v191
	s_add_u32 s54, s18, 0x80
	s_addc_u32 s55, s19, 0
	s_and_b64 s[22:23], exec, s[22:23]
	s_cselect_b32 s23, s1, s55
	s_cselect_b32 s22, s0, s54
	v_lshl_add_u64 v[16:17], s[18:19], 0, v[164:165]
	s_add_i32 m0, s27, 0xc000
	ds_read_b128 v[210:213], v202
	ds_read_b128 v[214:217], v202 offset:1024
	ds_read_b128 v[218:221], v202 offset:2048
	ds_read_b128 v[222:225], v202 offset:3072
	ds_read_b128 v[226:229], v202 offset:4096
	ds_read_b128 v[230:233], v202 offset:5120
	ds_read_b128 v[234:237], v202 offset:6144
	ds_read_b128 v[238:241], v202 offset:7168
	global_load_lds_dwordx4 v[16:17], off
	v_lshl_add_u64 v[16:17], s[18:19], 0, v[162:163]
	s_add_i32 m0, s27, 0xe000
	s_nop 0
	global_load_lds_dwordx4 v[16:17], off
	s_waitcnt lgkmcnt(8)
	s_barrier
	s_waitcnt lgkmcnt(0)
	s_setprio 1
	s_waitcnt lgkmcnt(0)
	v_mfma_scale_f32_16x16x128_f8f6f4 v[148:151], v[0:7], v[210:217], v[148:151], v203, v204 op_sel_hi:[0,0,0]
	v_mfma_scale_f32_16x16x128_f8f6f4 v[140:143], v[8:15], v[210:217], v[140:143], v203, v204 op_sel_hi:[0,0,0]
	v_mfma_scale_f32_16x16x128_f8f6f4 v[132:135], v[0:7], v[218:225], v[132:135], v203, v204 op_sel_hi:[0,0,0]
	v_mfma_scale_f32_16x16x128_f8f6f4 v[124:127], v[8:15], v[218:225], v[124:127], v203, v204 op_sel_hi:[0,0,0]
	v_mfma_scale_f32_16x16x128_f8f6f4 v[116:119], v[0:7], v[226:233], v[116:119], v203, v204 op_sel_hi:[0,0,0]
	v_mfma_scale_f32_16x16x128_f8f6f4 v[108:111], v[8:15], v[226:233], v[108:111], v203, v204 op_sel_hi:[0,0,0]
	v_mfma_scale_f32_16x16x128_f8f6f4 v[100:103], v[0:7], v[234:241], v[100:103], v203, v204 op_sel_hi:[0,0,0]
	v_mfma_scale_f32_16x16x128_f8f6f4 v[92:95], v[8:15], v[234:241], v[92:95], v203, v204 op_sel_hi:[0,0,0]
	s_setprio 0
	s_barrier
	s_mov_b32 m0, s28
	v_lshl_add_u64 v[172:173], s[20:21], 0, v[154:155]
	ds_read_b128 v[16:19], v185
	ds_read_b128 v[20:23], v192
	ds_read_b128 v[242:245], v193
	ds_read_b128 v[246:249], v194
	global_load_lds_dwordx4 v[172:173], off
	v_lshl_add_u64 v[174:175], s[20:21], 0, v[152:153]
	s_mov_b32 m0, s29
	s_nop 0
	global_load_lds_dwordx4 v[174:175], off
	s_barrier
	s_waitcnt lgkmcnt(0)
	s_setprio 1
	s_waitcnt lgkmcnt(0)
	v_mfma_scale_f32_16x16x128_f8f6f4 v[144:147], v[16:23], v[210:217], v[144:147], v209, v204 op_sel_hi:[0,0,0]
	v_mfma_scale_f32_16x16x128_f8f6f4 v[136:139], v[242:249], v[210:217], v[136:139], v209, v204 op_sel_hi:[0,0,0]
	v_mfma_scale_f32_16x16x128_f8f6f4 v[128:131], v[16:23], v[218:225], v[128:131], v209, v204 op_sel_hi:[0,0,0]
	v_mfma_scale_f32_16x16x128_f8f6f4 v[120:123], v[242:249], v[218:225], v[120:123], v209, v204 op_sel_hi:[0,0,0]
	v_mfma_scale_f32_16x16x128_f8f6f4 v[112:115], v[16:23], v[226:233], v[112:115], v209, v204 op_sel_hi:[0,0,0]
	v_mfma_scale_f32_16x16x128_f8f6f4 v[104:107], v[242:249], v[226:233], v[104:107], v209, v204 op_sel_hi:[0,0,0]
	v_mfma_scale_f32_16x16x128_f8f6f4 v[96:99], v[16:23], v[234:241], v[96:99], v209, v204 op_sel_hi:[0,0,0]
	v_mfma_scale_f32_16x16x128_f8f6f4 v[88:91], v[242:249], v[234:241], v[88:91], v209, v204 op_sel_hi:[0,0,0]
	s_setprio 0
	s_mov_b32 m0, s27
	s_barrier
	ds_read_b128 v[210:213], v202 offset:16384
	ds_read_b128 v[214:217], v202 offset:17408
	ds_read_b128 v[218:221], v202 offset:18432
	ds_read_b128 v[222:225], v202 offset:19456
	ds_read_b128 v[226:229], v202 offset:20480
	ds_read_b128 v[230:233], v202 offset:21504
	ds_read_b128 v[234:237], v202 offset:22528
	ds_read_b128 v[238:241], v202 offset:23552
	global_load_lds_dwordx4 v156, s[22:23]
	s_mov_b32 m0, s30
	v_mov_b32_e32 v177, v157
	global_load_lds_dwordx4 v176, s[22:23]
	s_barrier
	s_waitcnt lgkmcnt(0)
	v_lshl_add_u64 v[178:179], s[22:23], 0, v[156:157]
	v_lshl_add_u64 v[176:177], s[22:23], 0, v[176:177]
	s_setprio 1
	s_waitcnt lgkmcnt(0)
	v_mfma_scale_f32_16x16x128_f8f6f4 v[84:87], v[0:7], v[210:217], v[84:87], v203, v204 op_sel_hi:[0,0,0]
	v_mfma_scale_f32_16x16x128_f8f6f4 v[76:79], v[8:15], v[210:217], v[76:79], v203, v204 op_sel_hi:[0,0,0]
	v_mfma_scale_f32_16x16x128_f8f6f4 v[68:71], v[0:7], v[218:225], v[68:71], v203, v204 op_sel_hi:[0,0,0]
	v_mfma_scale_f32_16x16x128_f8f6f4 v[60:63], v[8:15], v[218:225], v[60:63], v203, v204 op_sel_hi:[0,0,0]
	v_mfma_scale_f32_16x16x128_f8f6f4 v[52:55], v[0:7], v[226:233], v[52:55], v203, v204 op_sel_hi:[0,0,0]
	v_mfma_scale_f32_16x16x128_f8f6f4 v[44:47], v[8:15], v[226:233], v[44:47], v203, v204 op_sel_hi:[0,0,0]
	v_mfma_scale_f32_16x16x128_f8f6f4 v[36:39], v[0:7], v[234:241], v[36:39], v203, v204 op_sel_hi:[0,0,0]
	v_mfma_scale_f32_16x16x128_f8f6f4 v[28:31], v[8:15], v[234:241], v[28:31], v203, v204 op_sel_hi:[0,0,0]
	s_setprio 0
	s_barrier
	s_add_u32 s54, s20, 0x40000
	s_addc_u32 s55, s21, 0
	s_mov_b32 m0, s31
	v_lshl_add_u64 v[0:1], s[54:55], 0, v[154:155]
	global_load_lds_dwordx4 v[0:1], off
	v_lshl_add_u64 v[0:1], s[54:55], 0, v[152:153]
	s_mov_b32 m0, s33
	s_nop 0
	global_load_lds_dwordx4 v[0:1], off
	s_waitcnt vmcnt(6)
	s_barrier
	s_setprio 1
	v_mfma_scale_f32_16x16x128_f8f6f4 v[80:83], v[16:23], v[210:217], v[80:83], v209, v204 op_sel_hi:[0,0,0]
	v_mfma_scale_f32_16x16x128_f8f6f4 v[72:75], v[242:249], v[210:217], v[72:75], v209, v204 op_sel_hi:[0,0,0]
	v_mfma_scale_f32_16x16x128_f8f6f4 v[64:67], v[16:23], v[218:225], v[64:67], v209, v204 op_sel_hi:[0,0,0]
	v_mfma_scale_f32_16x16x128_f8f6f4 v[56:59], v[242:249], v[218:225], v[56:59], v209, v204 op_sel_hi:[0,0,0]
	v_mfma_scale_f32_16x16x128_f8f6f4 v[48:51], v[16:23], v[226:233], v[48:51], v209, v204 op_sel_hi:[0,0,0]
	v_mfma_scale_f32_16x16x128_f8f6f4 v[40:43], v[242:249], v[226:233], v[40:43], v209, v204 op_sel_hi:[0,0,0]
	v_mfma_scale_f32_16x16x128_f8f6f4 v[32:35], v[16:23], v[234:241], v[32:35], v209, v204 op_sel_hi:[0,0,0]
	v_mfma_scale_f32_16x16x128_f8f6f4 v[24:27], v[242:249], v[234:241], v[24:27], v209, v204 op_sel_hi:[0,0,0]
	s_setprio 0
	s_barrier
	ds_read_b128 v[0:3], v186
	ds_read_b128 v[4:7], v195
	ds_read_b128 v[8:11], v196
	ds_read_b128 v[12:15], v197
	s_mov_b32 m0, s34
	v_lshl_add_u64 v[170:171], s[22:23], 0, v[170:171]
	ds_read_b128 v[16:19], v202 offset:32768
	ds_read_b128 v[20:23], v202 offset:33792
	ds_read_b128 v[210:213], v202 offset:34816
	ds_read_b128 v[214:217], v202 offset:35840
	ds_read_b128 v[218:221], v202 offset:36864
	ds_read_b128 v[222:225], v202 offset:37888
	ds_read_b128 v[226:229], v202 offset:38912
	ds_read_b128 v[230:233], v202 offset:39936
	global_load_lds_dwordx4 v[170:171], off
	v_lshl_add_u64 v[168:169], s[22:23], 0, v[168:169]
	s_mov_b32 m0, s35
	s_nop 0
	global_load_lds_dwordx4 v[168:169], off
	s_waitcnt lgkmcnt(8)
	s_barrier
	s_waitcnt lgkmcnt(0)
	s_setprio 1
	s_waitcnt lgkmcnt(0)
	v_mfma_scale_f32_16x16x128_f8f6f4 v[148:151], v[0:7], v[16:23], v[148:151], v203, v204 op_sel_hi:[0,0,0]
	v_mfma_scale_f32_16x16x128_f8f6f4 v[140:143], v[8:15], v[16:23], v[140:143], v203, v204 op_sel_hi:[0,0,0]
	v_mfma_scale_f32_16x16x128_f8f6f4 v[132:135], v[0:7], v[210:217], v[132:135], v203, v204 op_sel_hi:[0,0,0]
	v_mfma_scale_f32_16x16x128_f8f6f4 v[124:127], v[8:15], v[210:217], v[124:127], v203, v204 op_sel_hi:[0,0,0]
	v_mfma_scale_f32_16x16x128_f8f6f4 v[116:119], v[0:7], v[218:225], v[116:119], v203, v204 op_sel_hi:[0,0,0]
	v_mfma_scale_f32_16x16x128_f8f6f4 v[108:111], v[8:15], v[218:225], v[108:111], v203, v204 op_sel_hi:[0,0,0]
	v_mfma_scale_f32_16x16x128_f8f6f4 v[100:103], v[0:7], v[226:233], v[100:103], v203, v204 op_sel_hi:[0,0,0]
	v_mfma_scale_f32_16x16x128_f8f6f4 v[92:95], v[8:15], v[226:233], v[92:95], v203, v204 op_sel_hi:[0,0,0]
	s_setprio 0
	s_barrier
	s_mov_b32 m0, s36
	v_lshl_add_u64 v[168:169], v[172:173], 0, s[10:11]
	ds_read_b128 v[234:237], v187
	ds_read_b128 v[238:241], v198
	ds_read_b128 v[242:245], v199
	ds_read_b128 v[246:249], v200
	global_load_lds_dwordx4 v[168:169], off
	v_lshl_add_u64 v[168:169], v[174:175], 0, s[10:11]
	s_mov_b32 m0, s37
	s_nop 0
	global_load_lds_dwordx4 v[168:169], off
	s_barrier
	s_waitcnt lgkmcnt(0)
	s_setprio 1
	s_waitcnt lgkmcnt(0)
	v_mfma_scale_f32_16x16x128_f8f6f4 v[144:147], v[234:241], v[16:23], v[144:147], v209, v204 op_sel_hi:[0,0,0]
	v_mfma_scale_f32_16x16x128_f8f6f4 v[136:139], v[242:249], v[16:23], v[136:139], v209, v204 op_sel_hi:[0,0,0]
	v_mfma_scale_f32_16x16x128_f8f6f4 v[128:131], v[234:241], v[210:217], v[128:131], v209, v204 op_sel_hi:[0,0,0]
	v_mfma_scale_f32_16x16x128_f8f6f4 v[120:123], v[242:249], v[210:217], v[120:123], v209, v204 op_sel_hi:[0,0,0]
	v_mfma_scale_f32_16x16x128_f8f6f4 v[112:115], v[234:241], v[218:225], v[112:115], v209, v204 op_sel_hi:[0,0,0]
	v_mfma_scale_f32_16x16x128_f8f6f4 v[104:107], v[242:249], v[218:225], v[104:107], v209, v204 op_sel_hi:[0,0,0]
	v_mfma_scale_f32_16x16x128_f8f6f4 v[96:99], v[234:241], v[226:233], v[96:99], v209, v204 op_sel_hi:[0,0,0]
	v_mfma_scale_f32_16x16x128_f8f6f4 v[88:91], v[242:249], v[226:233], v[88:91], v209, v204 op_sel_hi:[0,0,0]
	s_setprio 0
	s_mov_b32 m0, s38
	v_lshl_add_u64 v[178:179], v[178:179], 0, s[10:11]
	s_barrier
	ds_read_b128 v[16:19], v202 offset:49152
	ds_read_b128 v[20:23], v202 offset:50176
	ds_read_b128 v[168:171], v202 offset:51200
	ds_read_b128 v[172:175], v202 offset:52224
	ds_read_b128 v[210:213], v202 offset:53248
	ds_read_b128 v[214:217], v202 offset:54272
	ds_read_b128 v[218:221], v202 offset:55296
	ds_read_b128 v[222:225], v202 offset:56320
	global_load_lds_dwordx4 v[178:179], off
	v_lshl_add_u64 v[176:177], v[176:177], 0, s[10:11]
	s_mov_b32 m0, s39
	s_nop 0
	global_load_lds_dwordx4 v[176:177], off
	s_barrier
	s_waitcnt lgkmcnt(0)
	s_setprio 1
	s_waitcnt lgkmcnt(0)
	v_mfma_scale_f32_16x16x128_f8f6f4 v[84:87], v[0:7], v[16:23], v[84:87], v203, v204 op_sel_hi:[0,0,0]
	v_mfma_scale_f32_16x16x128_f8f6f4 v[76:79], v[8:15], v[16:23], v[76:79], v203, v204 op_sel_hi:[0,0,0]
	v_mfma_scale_f32_16x16x128_f8f6f4 v[68:71], v[0:7], v[168:175], v[68:71], v203, v204 op_sel_hi:[0,0,0]
	v_mfma_scale_f32_16x16x128_f8f6f4 v[60:63], v[8:15], v[168:175], v[60:63], v203, v204 op_sel_hi:[0,0,0]
	v_mfma_scale_f32_16x16x128_f8f6f4 v[52:55], v[0:7], v[210:217], v[52:55], v203, v204 op_sel_hi:[0,0,0]
	v_mfma_scale_f32_16x16x128_f8f6f4 v[44:47], v[8:15], v[210:217], v[44:47], v203, v204 op_sel_hi:[0,0,0]
	v_mfma_scale_f32_16x16x128_f8f6f4 v[36:39], v[0:7], v[218:225], v[36:39], v203, v204 op_sel_hi:[0,0,0]
	v_mfma_scale_f32_16x16x128_f8f6f4 v[28:31], v[8:15], v[218:225], v[28:31], v203, v204 op_sel_hi:[0,0,0]
	s_setprio 0
	s_barrier
	s_add_u32 s20, s20, 0x40080
	s_addc_u32 s21, s21, 0
	s_mov_b32 m0, s40
	v_lshl_add_u64 v[0:1], s[20:21], 0, v[154:155]
	global_load_lds_dwordx4 v[0:1], off
	v_lshl_add_u64 v[0:1], s[20:21], 0, v[152:153]
	s_mov_b32 m0, s41
	s_nop 0
	global_load_lds_dwordx4 v[0:1], off
	s_waitcnt vmcnt(6)
	s_barrier
	s_setprio 1
	v_mfma_scale_f32_16x16x128_f8f6f4 v[80:83], v[234:241], v[16:23], v[80:83], v209, v204 op_sel_hi:[0,0,0]
	v_mfma_scale_f32_16x16x128_f8f6f4 v[72:75], v[242:249], v[16:23], v[72:75], v209, v204 op_sel_hi:[0,0,0]
	v_mfma_scale_f32_16x16x128_f8f6f4 v[64:67], v[234:241], v[168:175], v[64:67], v209, v204 op_sel_hi:[0,0,0]
	v_mfma_scale_f32_16x16x128_f8f6f4 v[56:59], v[242:249], v[168:175], v[56:59], v209, v204 op_sel_hi:[0,0,0]
	v_mfma_scale_f32_16x16x128_f8f6f4 v[48:51], v[234:241], v[210:217], v[48:51], v209, v204 op_sel_hi:[0,0,0]
	v_mfma_scale_f32_16x16x128_f8f6f4 v[40:43], v[242:249], v[210:217], v[40:43], v209, v204 op_sel_hi:[0,0,0]
	v_mfma_scale_f32_16x16x128_f8f6f4 v[32:35], v[234:241], v[218:225], v[32:35], v209, v204 op_sel_hi:[0,0,0]
	v_mfma_scale_f32_16x16x128_f8f6f4 v[24:27], v[242:249], v[218:225], v[24:27], v209, v204 op_sel_hi:[0,0,0]
	s_setprio 0
	s_add_i32 s53, s53, 2
	s_add_u32 s18, s18, 0x100
	s_addc_u32 s19, s19, 0
	s_add_u32 s16, s16, 0x100
	s_addc_u32 s17, s17, 0
	s_cmp_gt_u32 s53, 13
	s_cbranch_scc1 .Lrot9_exit
	s_cmp_eq_u32 s53, 12
	s_cselect_b64 s[22:23], -1, 0
	s_cbranch_scc1 .Lrot9_last
	v_mov_b64_e32 v[168:169], v[162:163]
	v_mov_b64_e32 v[170:171], v[164:165]
	v_mov_b32_e32 v176, v166
	v_mov_b32_e32 v156, v208
	s_mov_b64 s[20:21], s[16:17]
	s_barrier
	s_branch .LBB0_1335
.Lrot9_last:
	v_mov_b64_e32 v[168:169], v[160:161]
	v_mov_b64_e32 v[170:171], v[158:159]
	v_mov_b32_e32 v176, v207
	v_mov_b32_e32 v156, v206
	s_mov_b64 s[20:21], s[14:15]
	s_barrier
	s_branch .LBB0_1335
.Lrot9_exit:
	s_barrier
	s_branch .LBB0_1326
